# as v34 plus the P15 loop restructuring (double-buffered weight registers, spread loads, LDS-DMA activations) applied to the down-projection phase P16 too
# baseline (speedup 1.0000x reference)
.LBB0_1415:
	s_cmp_lt_i32 s68, 17
	s_cselect_b64 s[0:1], -1, 0
	s_cmp_gt_i32 s69, 16
	s_cselect_b64 s[2:3], -1, 0
	s_and_b64 s[0:1], s[0:1], s[2:3]
	s_andn2_b64 vcc, exec, s[0:1]
	s_cbranch_vccnz .LBB0_1518
	s_waitcnt vmcnt(0) lgkmcnt(0)
	v_mov_b32_e32 v3, v0
	v_and_b32_e32 v20, 63, v3
	v_lshlrev_b32_e32 v21, 2, v20
	global_load_dword v22, v21, s[94:95] sc1
	s_waitcnt vmcnt(0)
	v_lshlrev_b32_e32 v22, 6, v22
	v_sub_u32_e32 v23, 63, v20
	v_or_b32_e32 v22, v22, v23
	v_mov_b32_e32 v24, 0
	v_readlane_b32 s0, v22, 0
	s_nop 1
	v_cmp_gt_u32_e32 vcc, s0, v22
	s_nop 1
	v_addc_co_u32_e32 v24, vcc, 0, v24, vcc
	v_readlane_b32 s0, v22, 1
	s_nop 1
	v_cmp_gt_u32_e32 vcc, s0, v22
	s_nop 1
	v_addc_co_u32_e32 v24, vcc, 0, v24, vcc
	v_readlane_b32 s0, v22, 2
	s_nop 1
	v_cmp_gt_u32_e32 vcc, s0, v22
	s_nop 1
	v_addc_co_u32_e32 v24, vcc, 0, v24, vcc
	v_readlane_b32 s0, v22, 3
	s_nop 1
	v_cmp_gt_u32_e32 vcc, s0, v22
	s_nop 1
	v_addc_co_u32_e32 v24, vcc, 0, v24, vcc
	v_readlane_b32 s0, v22, 4
	s_nop 1
	v_cmp_gt_u32_e32 vcc, s0, v22
	s_nop 1
	v_addc_co_u32_e32 v24, vcc, 0, v24, vcc
	v_readlane_b32 s0, v22, 5
	s_nop 1
	v_cmp_gt_u32_e32 vcc, s0, v22
	s_nop 1
	v_addc_co_u32_e32 v24, vcc, 0, v24, vcc
	v_readlane_b32 s0, v22, 6
	s_nop 1
	v_cmp_gt_u32_e32 vcc, s0, v22
	s_nop 1
	v_addc_co_u32_e32 v24, vcc, 0, v24, vcc
	v_readlane_b32 s0, v22, 7
	s_nop 1
	v_cmp_gt_u32_e32 vcc, s0, v22
	s_nop 1
	v_addc_co_u32_e32 v24, vcc, 0, v24, vcc
	v_readlane_b32 s0, v22, 8
	s_nop 1
	v_cmp_gt_u32_e32 vcc, s0, v22
	s_nop 1
	v_addc_co_u32_e32 v24, vcc, 0, v24, vcc
	v_readlane_b32 s0, v22, 9
	s_nop 1
	v_cmp_gt_u32_e32 vcc, s0, v22
	s_nop 1
	v_addc_co_u32_e32 v24, vcc, 0, v24, vcc
	v_readlane_b32 s0, v22, 10
	s_nop 1
	v_cmp_gt_u32_e32 vcc, s0, v22
	s_nop 1
	v_addc_co_u32_e32 v24, vcc, 0, v24, vcc
	v_readlane_b32 s0, v22, 11
	s_nop 1
	v_cmp_gt_u32_e32 vcc, s0, v22
	s_nop 1
	v_addc_co_u32_e32 v24, vcc, 0, v24, vcc
	v_readlane_b32 s0, v22, 12
	s_nop 1
	v_cmp_gt_u32_e32 vcc, s0, v22
	s_nop 1
	v_addc_co_u32_e32 v24, vcc, 0, v24, vcc
	v_readlane_b32 s0, v22, 13
	s_nop 1
	v_cmp_gt_u32_e32 vcc, s0, v22
	s_nop 1
	v_addc_co_u32_e32 v24, vcc, 0, v24, vcc
	v_readlane_b32 s0, v22, 14
	s_nop 1
	v_cmp_gt_u32_e32 vcc, s0, v22
	s_nop 1
	v_addc_co_u32_e32 v24, vcc, 0, v24, vcc
	v_readlane_b32 s0, v22, 15
	s_nop 1
	v_cmp_gt_u32_e32 vcc, s0, v22
	s_nop 1
	v_addc_co_u32_e32 v24, vcc, 0, v24, vcc
	v_readlane_b32 s0, v22, 16
	s_nop 1
	v_cmp_gt_u32_e32 vcc, s0, v22
	s_nop 1
	v_addc_co_u32_e32 v24, vcc, 0, v24, vcc
	v_readlane_b32 s0, v22, 17
	s_nop 1
	v_cmp_gt_u32_e32 vcc, s0, v22
	s_nop 1
	v_addc_co_u32_e32 v24, vcc, 0, v24, vcc
	v_readlane_b32 s0, v22, 18
	s_nop 1
	v_cmp_gt_u32_e32 vcc, s0, v22
	s_nop 1
	v_addc_co_u32_e32 v24, vcc, 0, v24, vcc
	v_readlane_b32 s0, v22, 19
	s_nop 1
	v_cmp_gt_u32_e32 vcc, s0, v22
	s_nop 1
	v_addc_co_u32_e32 v24, vcc, 0, v24, vcc
	v_readlane_b32 s0, v22, 20
	s_nop 1
	v_cmp_gt_u32_e32 vcc, s0, v22
	s_nop 1
	v_addc_co_u32_e32 v24, vcc, 0, v24, vcc
	v_readlane_b32 s0, v22, 21
	s_nop 1
	v_cmp_gt_u32_e32 vcc, s0, v22
	s_nop 1
	v_addc_co_u32_e32 v24, vcc, 0, v24, vcc
	v_readlane_b32 s0, v22, 22
	s_nop 1
	v_cmp_gt_u32_e32 vcc, s0, v22
	s_nop 1
	v_addc_co_u32_e32 v24, vcc, 0, v24, vcc
	v_readlane_b32 s0, v22, 23
	s_nop 1
	v_cmp_gt_u32_e32 vcc, s0, v22
	s_nop 1
	v_addc_co_u32_e32 v24, vcc, 0, v24, vcc
	v_readlane_b32 s0, v22, 24
	s_nop 1
	v_cmp_gt_u32_e32 vcc, s0, v22
	s_nop 1
	v_addc_co_u32_e32 v24, vcc, 0, v24, vcc
	v_readlane_b32 s0, v22, 25
	s_nop 1
	v_cmp_gt_u32_e32 vcc, s0, v22
	s_nop 1
	v_addc_co_u32_e32 v24, vcc, 0, v24, vcc
	v_readlane_b32 s0, v22, 26
	s_nop 1
	v_cmp_gt_u32_e32 vcc, s0, v22
	s_nop 1
	v_addc_co_u32_e32 v24, vcc, 0, v24, vcc
	v_readlane_b32 s0, v22, 27
	s_nop 1
	v_cmp_gt_u32_e32 vcc, s0, v22
	s_nop 1
	v_addc_co_u32_e32 v24, vcc, 0, v24, vcc
	v_readlane_b32 s0, v22, 28
	s_nop 1
	v_cmp_gt_u32_e32 vcc, s0, v22
	s_nop 1
	v_addc_co_u32_e32 v24, vcc, 0, v24, vcc
	v_readlane_b32 s0, v22, 29
	s_nop 1
	v_cmp_gt_u32_e32 vcc, s0, v22
	s_nop 1
	v_addc_co_u32_e32 v24, vcc, 0, v24, vcc
	v_readlane_b32 s0, v22, 30
	s_nop 1
	v_cmp_gt_u32_e32 vcc, s0, v22
	s_nop 1
	v_addc_co_u32_e32 v24, vcc, 0, v24, vcc
	v_readlane_b32 s0, v22, 31
	s_nop 1
	v_cmp_gt_u32_e32 vcc, s0, v22
	s_nop 1
	v_addc_co_u32_e32 v24, vcc, 0, v24, vcc
	v_readlane_b32 s0, v22, 32
	s_nop 1
	v_cmp_gt_u32_e32 vcc, s0, v22
	s_nop 1
	v_addc_co_u32_e32 v24, vcc, 0, v24, vcc
	v_readlane_b32 s0, v22, 33
	s_nop 1
	v_cmp_gt_u32_e32 vcc, s0, v22
	s_nop 1
	v_addc_co_u32_e32 v24, vcc, 0, v24, vcc
	v_readlane_b32 s0, v22, 34
	s_nop 1
	v_cmp_gt_u32_e32 vcc, s0, v22
	s_nop 1
	v_addc_co_u32_e32 v24, vcc, 0, v24, vcc
	v_readlane_b32 s0, v22, 35
	s_nop 1
	v_cmp_gt_u32_e32 vcc, s0, v22
	s_nop 1
	v_addc_co_u32_e32 v24, vcc, 0, v24, vcc
	v_readlane_b32 s0, v22, 36
	s_nop 1
	v_cmp_gt_u32_e32 vcc, s0, v22
	s_nop 1
	v_addc_co_u32_e32 v24, vcc, 0, v24, vcc
	v_readlane_b32 s0, v22, 37
	s_nop 1
	v_cmp_gt_u32_e32 vcc, s0, v22
	s_nop 1
	v_addc_co_u32_e32 v24, vcc, 0, v24, vcc
	v_readlane_b32 s0, v22, 38
	s_nop 1
	v_cmp_gt_u32_e32 vcc, s0, v22
	s_nop 1
	v_addc_co_u32_e32 v24, vcc, 0, v24, vcc
	v_readlane_b32 s0, v22, 39
	s_nop 1
	v_cmp_gt_u32_e32 vcc, s0, v22
	s_nop 1
	v_addc_co_u32_e32 v24, vcc, 0, v24, vcc
	v_readlane_b32 s0, v22, 40
	s_nop 1
	v_cmp_gt_u32_e32 vcc, s0, v22
	s_nop 1
	v_addc_co_u32_e32 v24, vcc, 0, v24, vcc
	v_readlane_b32 s0, v22, 41
	s_nop 1
	v_cmp_gt_u32_e32 vcc, s0, v22
	s_nop 1
	v_addc_co_u32_e32 v24, vcc, 0, v24, vcc
	v_readlane_b32 s0, v22, 42
	s_nop 1
	v_cmp_gt_u32_e32 vcc, s0, v22
	s_nop 1
	v_addc_co_u32_e32 v24, vcc, 0, v24, vcc
	v_readlane_b32 s0, v22, 43
	s_nop 1
	v_cmp_gt_u32_e32 vcc, s0, v22
	s_nop 1
	v_addc_co_u32_e32 v24, vcc, 0, v24, vcc
	v_readlane_b32 s0, v22, 44
	s_nop 1
	v_cmp_gt_u32_e32 vcc, s0, v22
	s_nop 1
	v_addc_co_u32_e32 v24, vcc, 0, v24, vcc
	v_readlane_b32 s0, v22, 45
	s_nop 1
	v_cmp_gt_u32_e32 vcc, s0, v22
	s_nop 1
	v_addc_co_u32_e32 v24, vcc, 0, v24, vcc
	v_readlane_b32 s0, v22, 46
	s_nop 1
	v_cmp_gt_u32_e32 vcc, s0, v22
	s_nop 1
	v_addc_co_u32_e32 v24, vcc, 0, v24, vcc
	v_readlane_b32 s0, v22, 47
	s_nop 1
	v_cmp_gt_u32_e32 vcc, s0, v22
	s_nop 1
	v_addc_co_u32_e32 v24, vcc, 0, v24, vcc
	v_readlane_b32 s0, v22, 48
	s_nop 1
	v_cmp_gt_u32_e32 vcc, s0, v22
	s_nop 1
	v_addc_co_u32_e32 v24, vcc, 0, v24, vcc
	v_readlane_b32 s0, v22, 49
	s_nop 1
	v_cmp_gt_u32_e32 vcc, s0, v22
	s_nop 1
	v_addc_co_u32_e32 v24, vcc, 0, v24, vcc
	v_readlane_b32 s0, v22, 50
	s_nop 1
	v_cmp_gt_u32_e32 vcc, s0, v22
	s_nop 1
	v_addc_co_u32_e32 v24, vcc, 0, v24, vcc
	v_readlane_b32 s0, v22, 51
	s_nop 1
	v_cmp_gt_u32_e32 vcc, s0, v22
	s_nop 1
	v_addc_co_u32_e32 v24, vcc, 0, v24, vcc
	v_readlane_b32 s0, v22, 52
	s_nop 1
	v_cmp_gt_u32_e32 vcc, s0, v22
	s_nop 1
	v_addc_co_u32_e32 v24, vcc, 0, v24, vcc
	v_readlane_b32 s0, v22, 53
	s_nop 1
	v_cmp_gt_u32_e32 vcc, s0, v22
	s_nop 1
	v_addc_co_u32_e32 v24, vcc, 0, v24, vcc
	v_readlane_b32 s0, v22, 54
	s_nop 1
	v_cmp_gt_u32_e32 vcc, s0, v22
	s_nop 1
	v_addc_co_u32_e32 v24, vcc, 0, v24, vcc
	v_readlane_b32 s0, v22, 55
	s_nop 1
	v_cmp_gt_u32_e32 vcc, s0, v22
	s_nop 1
	v_addc_co_u32_e32 v24, vcc, 0, v24, vcc
	v_readlane_b32 s0, v22, 56
	s_nop 1
	v_cmp_gt_u32_e32 vcc, s0, v22
	s_nop 1
	v_addc_co_u32_e32 v24, vcc, 0, v24, vcc
	v_readlane_b32 s0, v22, 57
	s_nop 1
	v_cmp_gt_u32_e32 vcc, s0, v22
	s_nop 1
	v_addc_co_u32_e32 v24, vcc, 0, v24, vcc
	v_readlane_b32 s0, v22, 58
	s_nop 1
	v_cmp_gt_u32_e32 vcc, s0, v22
	s_nop 1
	v_addc_co_u32_e32 v24, vcc, 0, v24, vcc
	v_readlane_b32 s0, v22, 59
	s_nop 1
	v_cmp_gt_u32_e32 vcc, s0, v22
	s_nop 1
	v_addc_co_u32_e32 v24, vcc, 0, v24, vcc
	v_readlane_b32 s0, v22, 60
	s_nop 1
	v_cmp_gt_u32_e32 vcc, s0, v22
	s_nop 1
	v_addc_co_u32_e32 v24, vcc, 0, v24, vcc
	v_readlane_b32 s0, v22, 61
	s_nop 1
	v_cmp_gt_u32_e32 vcc, s0, v22
	s_nop 1
	v_addc_co_u32_e32 v24, vcc, 0, v24, vcc
	v_readlane_b32 s0, v22, 62
	s_nop 1
	v_cmp_gt_u32_e32 vcc, s0, v22
	s_nop 1
	v_addc_co_u32_e32 v24, vcc, 0, v24, vcc
	v_readlane_b32 s0, v22, 63
	s_nop 1
	v_cmp_gt_u32_e32 vcc, s0, v22
	s_nop 1
	v_addc_co_u32_e32 v24, vcc, 0, v24, vcc
	s_lshr_b32 s1, s65, 4
	v_cmp_eq_u32_e32 vcc, s1, v24
	s_nop 3
	s_ff1_i32_b64 s100, vcc
	s_sub_i32 s2, 31, s1
	v_cmp_eq_u32_e32 vcc, s2, v24
	s_nop 3
	s_ff1_i32_b64 s0, vcc
	s_lshl_b32 s0, s0, 8
	s_or_b32 s100, s100, s0
	s_add_i32 s2, s1, 32
	v_cmp_eq_u32_e32 vcc, s2, v24
	s_nop 3
	s_ff1_i32_b64 s0, vcc
	s_lshl_b32 s0, s0, 16
	s_or_b32 s100, s100, s0
	s_sub_i32 s2, 63, s1
	v_cmp_eq_u32_e32 vcc, s2, v24
	s_nop 3
	s_ff1_i32_b64 s0, vcc
	s_lshl_b32 s0, s0, 24
	s_or_b32 s100, s100, s0
	s_cmpk_gt_i32 s65, 0x3ff
	v_and_b32_e32 v2, 15, v3
	v_mul_lo_u32 v1, v2, s33
	v_add_u32_e32 v1, s65, v1
	v_lshrrev_b32_e32 v1, 2, v1
	v_and_b32_e32 v4, 0xfc, v1
	v_and_b32_e32 v20, 3, v2
	v_lshlrev_b32_e32 v20, 3, v20
	v_lshrrev_b32_e64 v4, v20, s100
	v_and_b32_e32 v4, 0xff, v4
	v_lshlrev_b32_e32 v4, 2, v4
	global_load_dword v1, v4, s[94:95] sc1
	global_load_dword v172, v4, s[94:95] offset:256 sc1
	s_cbranch_scc1 .LBB0_1464
	s_add_u32 s24, s94, 0x4b000000
	s_addc_u32 s25, s95, 0
	s_add_u32 s0, s94, 0x4f000000
	v_readlane_b32 s2, v254, 0
	s_addc_u32 s1, s95, 0
	v_bfe_u32 v4, v3, 4, 2
	s_lshr_b32 s2, s2, 8
	v_lshlrev_b32_e32 v5, 4, v2
	v_lshlrev_b32_e32 v6, 4, v3
	s_lshl_b32 s3, s2, 1
	v_lshl_or_b32 v173, v4, 15, v5
	v_ashrrev_i32_e32 v5, 3, v3
	v_and_b32_e32 v6, 0x70, v6
	s_add_i32 s3, s3, s97
	v_lshl_or_b32 v174, v5, 11, v6
	v_lshlrev_b32_e32 v6, 7, v5
	v_xor_b32_e32 v5, v5, v3
	v_bfe_u32 v175, v3, 5, 1
	v_and_b32_e32 v10, 7, v3
	v_lshlrev_b32_e32 v11, 2, v3
	v_bitop3_b32 v3, v4, v3, 7 bitop3:0x78
	v_lshrrev_b32_e32 v13, 2, v2
	s_and_b32 s26, s3, 3
	v_xor_b32_e32 v13, v3, v13
	v_lshlrev_b32_e32 v12, 7, v2
	s_lshl_b32 s3, s26, 11
	s_lshl_b32 s4, s2, 13
	v_lshlrev_b32_e32 v13, 4, v13
	v_lshl_add_u32 v3, v3, 4, 0
	v_lshlrev_b32_e32 v5, 4, v5
	v_lshlrev_b32_e32 v8, 3, v4
	v_add3_u32 v176, v3, v12, s3
	v_or3_b32 v3, v13, s4, v12
	v_and_b32_e32 v5, 0x70, v5
	v_lshlrev_b32_e32 v7, 9, v2
	v_bitop3_b32 v4, v4, v10, 4 bitop3:0x36
	s_add_i32 s5, s4, 0xc000
	v_add_u32_e32 v3, 0, v3
	v_lshl_or_b32 v201, v2, 12, v8
	v_mov_b32_e32 v2, 0
	v_and_b32_e32 v9, 8, v8
	v_or3_b32 v14, v13, s5, v12
	v_add_u32_e32 v178, 0xc000, v3
	v_add_u32_e32 v179, 0x1c000, v3
	v_lshl_add_u32 v3, v4, 4, 0
	v_add3_u32 v184, 0, v5, v6
	v_sub_u32_e32 v187, v184, v5
	v_lshl_or_b32 v187, v187, 4, v5
	s_mul_i32 s98, s97, 0x400
	s_mov_b32 s99, s98
	s_bitset1_b32 s99, 16
	v_mov_b32_e32 v4, v2
	v_mov_b32_e32 v5, v2
	v_add3_u32 v180, v3, v12, s3
	v_xad_u32 v182, v14, 64, 0
	v_add3_u32 v185, 0, v7, v9
	v_bitop3_b32 v192, v11, v10, 4 bitop3:0x6c
	v_mov_b32_e32 v3, v2
	v_mbcnt_lo_u32_b32 v6, -1, 0
	v_mov_b64_e32 v[18:19], v[4:5]
	v_mov_b64_e32 v[14:15], v[4:5]
	v_mov_b64_e32 v[10:11], v[4:5]
	s_mov_b32 s7, 0x20000
	s_or_b32 s30, s26, 4
	s_or_b32 s34, s26, 8
	s_or_b32 s36, s26, 12
	s_or_b32 s38, s26, 16
	v_mbcnt_hi_u32_b32 v193, -1, v6
	v_mov_b64_e32 v[16:17], v[2:3]
	v_mov_b64_e32 v[12:13], v[2:3]
	v_mov_b64_e32 v[8:9], v[2:3]
	v_mov_b64_e32 v[6:7], v[4:5]
	s_mov_b32 s27, 0
	v_add_u32_e32 v177, 0x10000, v176
	v_add_u32_e32 v181, 0x10000, v180
	v_add_u32_e32 v183, 0x10000, v182
	v_add_u32_e32 v186, 0x10000, v184
	s_and_b32 s1, s1, 0xffff
	s_brev_b32 s10, -2
	s_mov_b32 s11, s7
	s_lshl_b32 s28, s26, 15
	s_lshl_b32 s29, s2, 7
	s_lshl_b32 s31, s30, 15
	s_lshl_b32 s35, s34, 15
	s_lshl_b32 s37, s36, 15
	s_lshl_b32 s39, s38, 15
	s_mov_b64 s[16:17], 0
	s_mov_b32 s40, 0x40000
	s_mov_b32 s41, 0x60000
	s_mov_b32 s42, 0x80000
	s_movk_i32 s43, 0x2000
	s_movk_i32 s44, 0x4000
	s_movk_i32 s45, 0x6000
	s_movk_i32 s46, 0x80
	s_mov_b32 s47, 0x20080
	s_mov_b32 s48, 0x40080
	s_mov_b32 s49, 0x60080
	s_mov_b32 s50, 0x80080
	s_mov_b32 s51, 0x82000
	s_mov_b32 s52, 0x84000
	s_mov_b32 s53, 0x86000
	v_mov_b64_e32 v[4:5], v[2:3]
	s_branch .LBB0_1419

.LBB0_1429:
	buffer_load_dwordx4 v[242:245], v173, s[8:11], s42 offen
	buffer_load_dwordx4 v[246:249], v173, s[8:11], s51 offen
	buffer_load_dwordx4 v[250:253], v173, s[8:11], s52 offen
	buffer_load_dwordx4 v[188:191], v173, s[8:11], s53 offen
	s_waitcnt vmcnt(4)
	ds_write_b128 v184, v[36:39]
	ds_write_b128 v184, v[40:43] offset:8192
	ds_write_b128 v184, v[44:47] offset:16384
	ds_write_b128 v184, v[48:51] offset:24576
	ds_write_b128 v184, v[52:55] offset:32768
	v_cvt_pk_bf16_f32 v36, v32, v28
	v_cvt_pk_bf16_f32 v37, v24, v20
	ds_write_b64 v3, v[36:37] offset:49152
	v_cvt_pk_bf16_f32 v20, v33, v29
	v_cvt_pk_bf16_f32 v21, v25, v21
	ds_write_b64 v194, v[20:21] offset:49280
	v_cvt_pk_bf16_f32 v20, v34, v30
	v_cvt_pk_bf16_f32 v21, v26, v22
	ds_write_b64 v195, v[20:21] offset:49408
	v_cvt_pk_bf16_f32 v20, v35, v31
	v_cvt_pk_bf16_f32 v21, v27, v23
	ds_write_b64 v196, v[20:21] offset:49536
	s_waitcnt lgkmcnt(0)
	s_barrier
	s_mov_b32 m0, s99
	s_nop 0
	buffer_load_dwordx4 v187, s[4:7], s46 offen lds
	s_add_i32 m0, s99, 0x2000
	s_nop 0
	buffer_load_dwordx4 v187, s[4:7], s47 offen lds
	s_add_i32 m0, s99, 0x4000
	s_nop 0
	buffer_load_dwordx4 v187, s[4:7], s48 offen lds
	s_add_i32 m0, s99, 0x6000
	s_nop 0
	buffer_load_dwordx4 v187, s[4:7], s49 offen lds
	s_add_i32 m0, s99, 0x8000
	s_nop 0
	buffer_load_dwordx4 v187, s[4:7], s50 offen lds
	ds_read_b128 v[92:95], v176 offset:0
	ds_read_b128 v[76:79], v176 offset:0x2000
	ds_read_b128 v[64:67], v176 offset:0x4000
	ds_read_b128 v[60:63], v176 offset:0x6000
	ds_read_b128 v[56:59], v176 offset:0x8000
	ds_read_b128 v[68:71], v178 offset:0
	ds_read_b128 v[72:75], v182 offset:0x800
	ds_read_b128 v[80:83], v178 offset:0x1000
	ds_read_b128 v[84:87], v182 offset:0x1800
	v_mov_b32_e32 v88, 0
	s_mov_b32 s2, -2
	s_mov_b32 s3, 0x186000
	s_mov_b32 s14, 0x80180
	v_mov_b32_e32 v89, v88
	v_mov_b32_e32 v90, v88
	v_mov_b32_e32 v91, v88
	v_mov_b32_e32 v96, v88
	v_mov_b32_e32 v97, v88
	v_mov_b32_e32 v98, v88
	v_mov_b32_e32 v99, v88
	v_mov_b32_e32 v100, v88
	v_mov_b32_e32 v101, v88
	v_mov_b32_e32 v102, v88
	v_mov_b32_e32 v103, v88
	v_mov_b32_e32 v104, v88
	v_mov_b32_e32 v105, v88
	v_mov_b32_e32 v106, v88
	v_mov_b32_e32 v107, v88
	v_mov_b32_e32 v108, v88
	v_mov_b32_e32 v109, v88
	v_mov_b32_e32 v110, v88
	v_mov_b32_e32 v111, v88
	v_mov_b32_e32 v112, v88
	v_mov_b32_e32 v113, v88
	v_mov_b32_e32 v114, v88
	v_mov_b32_e32 v115, v88
	v_mov_b32_e32 v116, v88
	v_mov_b32_e32 v117, v88
	v_mov_b32_e32 v118, v88
	v_mov_b32_e32 v119, v88
	v_mov_b32_e32 v120, v88
	v_mov_b32_e32 v121, v88
	v_mov_b32_e32 v122, v88
	v_mov_b32_e32 v123, v88
	v_mov_b32_e32 v124, v88
	v_mov_b32_e32 v125, v88
	v_mov_b32_e32 v126, v88
	v_mov_b32_e32 v127, v88
	v_mov_b32_e32 v128, v88
	v_mov_b32_e32 v129, v88
	v_mov_b32_e32 v130, v88
	v_mov_b32_e32 v131, v88
	v_mov_b32_e32 v132, v88
	v_mov_b32_e32 v133, v88
	v_mov_b32_e32 v134, v88
	v_mov_b32_e32 v135, v88
	v_mov_b32_e32 v136, v88
	v_mov_b32_e32 v137, v88
	v_mov_b32_e32 v138, v88
	v_mov_b32_e32 v139, v88
	v_mov_b32_e32 v140, v88
	v_mov_b32_e32 v141, v88
	v_mov_b32_e32 v142, v88
	v_mov_b32_e32 v143, v88
	v_mov_b32_e32 v144, v88
	v_mov_b32_e32 v145, v88
	v_mov_b32_e32 v146, v88
	v_mov_b32_e32 v147, v88
	v_mov_b32_e32 v148, v88
	v_mov_b32_e32 v149, v88
	v_mov_b32_e32 v150, v88
	v_mov_b32_e32 v151, v88
	v_mov_b32_e32 v152, v88
	v_mov_b32_e32 v153, v88
	v_mov_b32_e32 v154, v88
	v_mov_b32_e32 v155, v88
	v_mov_b32_e32 v156, v88
	v_mov_b32_e32 v157, v88
	v_mov_b32_e32 v158, v88
	v_mov_b32_e32 v159, v88
	v_mov_b32_e32 v160, v88
	v_mov_b32_e32 v161, v88
	v_mov_b32_e32 v162, v88
	v_mov_b32_e32 v163, v88
	v_mov_b32_e32 v164, v88
	v_mov_b32_e32 v165, v88
	v_mov_b32_e32 v166, v88
	v_mov_b32_e32 v167, v88
	v_mov_b32_e32 v168, v88
	v_mov_b32_e32 v169, v88
	v_mov_b32_e32 v170, v88
	v_mov_b32_e32 v171, v88
.LBB0_1430:
	ds_read_b128 v[202:205], v180 offset:0
	ds_read_b128 v[206:209], v180 offset:0x2000
	ds_read_b128 v[210:213], v180 offset:0x4000
	ds_read_b128 v[214:217], v180 offset:0x6000
	ds_read_b128 v[218:221], v180 offset:0x8000
	ds_read_b128 v[222:225], v182 offset:0
	ds_read_b128 v[226:229], v178 offset:0x800
	ds_read_b128 v[230:233], v182 offset:0x1000
	ds_read_b128 v[234:237], v178 offset:0x1800
	s_waitcnt lgkmcnt(9)
	s_nop 1
	v_mfma_f32_16x16x32_bf16 v[168:171], v[68:71], v[92:95], v[168:171]
	v_mfma_f32_16x16x32_bf16 v[164:167], v[72:75], v[92:95], v[164:167]
	s_add_i32 s15, s3, 0xfff7a000
	buffer_load_dwordx4 v[24:27], v173, s[8:11], s15 offen
	v_mfma_f32_16x16x32_bf16 v[160:163], v[80:83], v[92:95], v[160:163]
	v_mfma_f32_16x16x32_bf16 v[92:95], v[84:87], v[92:95], v[156:159]
	v_mfma_f32_16x16x32_bf16 v[152:155], v[68:71], v[76:79], v[152:155]
	v_mfma_f32_16x16x32_bf16 v[148:151], v[72:75], v[76:79], v[148:151]
	v_mfma_f32_16x16x32_bf16 v[144:147], v[80:83], v[76:79], v[144:147]
	s_add_i32 s65, s3, 0xfff7c000
	buffer_load_dwordx4 v[32:35], v173, s[8:11], s65 offen
	v_mfma_f32_16x16x32_bf16 v[76:79], v[84:87], v[76:79], v[140:143]
	v_mfma_f32_16x16x32_bf16 v[136:139], v[68:71], v[64:67], v[136:139]
	v_mfma_f32_16x16x32_bf16 v[132:135], v[72:75], v[64:67], v[132:135]
	v_mfma_f32_16x16x32_bf16 v[128:131], v[80:83], v[64:67], v[128:131]
	v_mfma_f32_16x16x32_bf16 v[64:67], v[84:87], v[64:67], v[124:127]
	s_add_i32 s15, s3, 0xfff7e000
	buffer_load_dwordx4 v[20:23], v173, s[8:11], s15 offen
	v_mfma_f32_16x16x32_bf16 v[120:123], v[68:71], v[60:63], v[120:123]
	v_mfma_f32_16x16x32_bf16 v[116:119], v[72:75], v[60:63], v[116:119]
	v_mfma_f32_16x16x32_bf16 v[112:115], v[80:83], v[60:63], v[112:115]
	v_mfma_f32_16x16x32_bf16 v[60:63], v[84:87], v[60:63], v[108:111]
	v_mfma_f32_16x16x32_bf16 v[68:71], v[68:71], v[56:59], v[104:107]
	s_add_i32 s65, s3, 0xfff80000
	buffer_load_dwordx4 v[28:31], v173, s[8:11], s65 offen
	v_mfma_f32_16x16x32_bf16 v[72:75], v[72:75], v[56:59], v[100:103]
	v_mfma_f32_16x16x32_bf16 v[80:83], v[80:83], v[56:59], v[96:99]
	v_mfma_f32_16x16x32_bf16 v[56:59], v[84:87], v[56:59], v[88:91]
	s_waitcnt vmcnt(4)
	v_cvt_pk_bf16_f32 v36, v242, v246
	v_cvt_pk_bf16_f32 v37, v250, v188
	ds_write_b64 v197, v[36:37]
	v_cvt_pk_bf16_f32 v36, v243, v247
	v_cvt_pk_bf16_f32 v37, v251, v189
	ds_write_b64 v198, v[36:37]
	v_cvt_pk_bf16_f32 v36, v244, v248
	v_cvt_pk_bf16_f32 v37, v252, v190
	ds_write_b64 v199, v[36:37]
	v_cvt_pk_bf16_f32 v36, v245, v249
	v_cvt_pk_bf16_f32 v37, v253, v191
	ds_write_b64 v200, v[36:37]
	s_waitcnt lgkmcnt(0)
	s_barrier
	s_nop 0
	v_mfma_f32_16x16x32_bf16 v[124:127], v[222:225], v[210:213], v[136:139]
	ds_read_b128 v[136:139], v177 offset:0
	ds_read_b128 v[140:143], v177 offset:0x2000
	v_mfma_f32_16x16x32_bf16 v[108:111], v[230:233], v[206:209], v[144:147]
	s_mov_b32 m0, s98
	s_add_i32 s15, s14, 0xfff7ff80
	buffer_load_dwordx4 v187, s[4:7], s15 offen lds
	ds_read_b128 v[144:147], v177 offset:0x4000
	v_mfma_f32_16x16x32_bf16 v[104:107], v[226:229], v[206:209], v[148:151]
	ds_read_b128 v[148:151], v177 offset:0x6000
	v_mfma_f32_16x16x32_bf16 v[100:103], v[222:225], v[206:209], v[152:155]
	ds_read_b128 v[152:155], v177 offset:0x8000
	ds_read_b128 v[156:159], v179 offset:0
	v_mfma_f32_16x16x32_bf16 v[96:99], v[230:233], v[202:205], v[160:163]
	ds_read_b128 v[160:163], v183 offset:0x800
	v_mfma_f32_16x16x32_bf16 v[84:87], v[222:225], v[202:205], v[168:171]
	s_add_i32 m0, s98, 0x2000
	s_add_i32 s65, s14, 0xfff9ff80
	buffer_load_dwordx4 v187, s[4:7], s65 offen lds
	v_mfma_f32_16x16x32_bf16 v[88:91], v[226:229], v[202:205], v[164:167]
	ds_read_b128 v[164:167], v179 offset:0x1000
	ds_read_b128 v[168:171], v183 offset:0x1800
	v_mfma_f32_16x16x32_bf16 v[92:95], v[234:237], v[202:205], v[92:95]
	v_mfma_f32_16x16x32_bf16 v[76:79], v[234:237], v[206:209], v[76:79]
	v_mfma_f32_16x16x32_bf16 v[132:135], v[226:229], v[210:213], v[132:135]
	s_add_i32 m0, s98, 0x4000
	s_add_i32 s15, s14, 0xfffbff80
	buffer_load_dwordx4 v187, s[4:7], s15 offen lds
	v_mfma_f32_16x16x32_bf16 v[128:131], v[230:233], v[210:213], v[128:131]
	v_mfma_f32_16x16x32_bf16 v[64:67], v[234:237], v[210:213], v[64:67]
	v_mfma_f32_16x16x32_bf16 v[120:123], v[222:225], v[214:217], v[120:123]
	v_mfma_f32_16x16x32_bf16 v[116:119], v[226:229], v[214:217], v[116:119]
	s_add_i32 m0, s98, 0x6000
	s_add_i32 s65, s14, 0xfffdff80
	buffer_load_dwordx4 v187, s[4:7], s65 offen lds
	v_mfma_f32_16x16x32_bf16 v[112:115], v[230:233], v[214:217], v[112:115]
	v_mfma_f32_16x16x32_bf16 v[60:63], v[234:237], v[214:217], v[60:63]
	v_mfma_f32_16x16x32_bf16 v[68:71], v[222:225], v[218:221], v[68:71]
	v_mfma_f32_16x16x32_bf16 v[72:75], v[226:229], v[218:221], v[72:75]
	s_add_i32 m0, s98, 0x8000
	s_add_i32 s15, s14, 0xffffff80
	buffer_load_dwordx4 v187, s[4:7], s15 offen lds
	v_mfma_f32_16x16x32_bf16 v[80:83], v[230:233], v[218:221], v[80:83]
	v_mfma_f32_16x16x32_bf16 v[56:59], v[234:237], v[218:221], v[56:59]
	ds_read_b128 v[202:205], v181 offset:0
	ds_read_b128 v[206:209], v181 offset:0x2000
	ds_read_b128 v[210:213], v181 offset:0x4000
	ds_read_b128 v[214:217], v181 offset:0x6000
	ds_read_b128 v[218:221], v181 offset:0x8000
	ds_read_b128 v[222:225], v183 offset:0
	ds_read_b128 v[226:229], v179 offset:0x800
	ds_read_b128 v[230:233], v183 offset:0x1000
	ds_read_b128 v[234:237], v179 offset:0x1800
	s_waitcnt lgkmcnt(9)
	s_nop 0
	v_mfma_f32_16x16x32_bf16 v[84:87], v[156:159], v[136:139], v[84:87]
	v_mfma_f32_16x16x32_bf16 v[88:91], v[160:163], v[136:139], v[88:91]
	s_add_i32 s15, s3, 0xffffa000
	buffer_load_dwordx4 v[242:245], v173, s[8:11], s15 offen
	v_mfma_f32_16x16x32_bf16 v[96:99], v[164:167], v[136:139], v[96:99]
	v_mfma_f32_16x16x32_bf16 v[92:95], v[168:171], v[136:139], v[92:95]
	v_mfma_f32_16x16x32_bf16 v[100:103], v[156:159], v[140:143], v[100:103]
	v_mfma_f32_16x16x32_bf16 v[104:107], v[160:163], v[140:143], v[104:107]
	v_mfma_f32_16x16x32_bf16 v[108:111], v[164:167], v[140:143], v[108:111]
	s_add_i32 s65, s3, 0xffffc000
	buffer_load_dwordx4 v[246:249], v173, s[8:11], s65 offen
	v_mfma_f32_16x16x32_bf16 v[76:79], v[168:171], v[140:143], v[76:79]
	v_mfma_f32_16x16x32_bf16 v[124:127], v[156:159], v[144:147], v[124:127]
	v_mfma_f32_16x16x32_bf16 v[132:135], v[160:163], v[144:147], v[132:135]
	v_mfma_f32_16x16x32_bf16 v[128:131], v[164:167], v[144:147], v[128:131]
	v_mfma_f32_16x16x32_bf16 v[64:67], v[168:171], v[144:147], v[64:67]
	s_add_i32 s15, s3, 0xffffe000
	buffer_load_dwordx4 v[250:253], v173, s[8:11], s15 offen
	v_mfma_f32_16x16x32_bf16 v[120:123], v[156:159], v[148:151], v[120:123]
	v_mfma_f32_16x16x32_bf16 v[116:119], v[160:163], v[148:151], v[116:119]
	v_mfma_f32_16x16x32_bf16 v[112:115], v[164:167], v[148:151], v[112:115]
	v_mfma_f32_16x16x32_bf16 v[60:63], v[168:171], v[148:151], v[60:63]
	v_mfma_f32_16x16x32_bf16 v[68:71], v[156:159], v[152:155], v[68:71]
	buffer_load_dwordx4 v[188:191], v173, s[8:11], s3 offen
	v_mfma_f32_16x16x32_bf16 v[72:75], v[160:163], v[152:155], v[72:75]
	v_mfma_f32_16x16x32_bf16 v[80:83], v[164:167], v[152:155], v[80:83]
	v_mfma_f32_16x16x32_bf16 v[238:241], v[168:171], v[152:155], v[56:59]
	s_waitcnt vmcnt(4)
	v_cvt_pk_bf16_f32 v36, v24, v32
	v_cvt_pk_bf16_f32 v37, v20, v28
	ds_write_b64 v3, v[36:37] offset:49152
	v_cvt_pk_bf16_f32 v36, v25, v33
	v_cvt_pk_bf16_f32 v37, v21, v29
	ds_write_b64 v194, v[36:37] offset:49280
	v_cvt_pk_bf16_f32 v36, v26, v34
	v_cvt_pk_bf16_f32 v37, v22, v30
	ds_write_b64 v195, v[36:37] offset:49408
	v_cvt_pk_bf16_f32 v36, v27, v35
	v_cvt_pk_bf16_f32 v37, v23, v31
	ds_write_b64 v196, v[36:37] offset:49536
	s_waitcnt lgkmcnt(0)
	s_barrier
	s_nop 0
	v_mfma_f32_16x16x32_bf16 v[156:159], v[234:237], v[202:205], v[92:95]
	ds_read_b128 v[92:95], v176 offset:0
	v_mfma_f32_16x16x32_bf16 v[140:143], v[234:237], v[206:209], v[76:79]
	s_mov_b32 m0, s99
	s_add_i32 s15, s14, 0xfff80000
	buffer_load_dwordx4 v187, s[4:7], s15 offen lds
	ds_read_b128 v[76:79], v176 offset:0x2000
	v_mfma_f32_16x16x32_bf16 v[136:139], v[222:225], v[210:213], v[124:127]
	v_mfma_f32_16x16x32_bf16 v[124:127], v[234:237], v[210:213], v[64:67]
	ds_read_b128 v[64:67], v176 offset:0x4000
	v_mfma_f32_16x16x32_bf16 v[144:147], v[230:233], v[206:209], v[108:111]
	v_mfma_f32_16x16x32_bf16 v[108:111], v[234:237], v[214:217], v[60:63]
	s_add_i32 m0, s99, 0x2000
	s_add_i32 s65, s14, 0xfffa0000
	buffer_load_dwordx4 v187, s[4:7], s65 offen lds
	ds_read_b128 v[60:63], v176 offset:0x6000
	ds_read_b128 v[56:59], v176 offset:0x8000
	v_mfma_f32_16x16x32_bf16 v[148:151], v[226:229], v[206:209], v[104:107]
	v_mfma_f32_16x16x32_bf16 v[104:107], v[222:225], v[218:221], v[68:71]
	ds_read_b128 v[68:71], v178 offset:0
	v_mfma_f32_16x16x32_bf16 v[152:155], v[222:225], v[206:209], v[100:103]
	v_mfma_f32_16x16x32_bf16 v[100:103], v[226:229], v[218:221], v[72:75]
	s_add_i32 m0, s99, 0x4000
	s_add_i32 s15, s14, 0xfffc0000
	buffer_load_dwordx4 v187, s[4:7], s15 offen lds
	ds_read_b128 v[72:75], v182 offset:0x800
	v_mfma_f32_16x16x32_bf16 v[168:171], v[222:225], v[202:205], v[84:87]
	v_mfma_f32_16x16x32_bf16 v[164:167], v[226:229], v[202:205], v[88:91]
	v_mfma_f32_16x16x32_bf16 v[160:163], v[230:233], v[202:205], v[96:99]
	v_mfma_f32_16x16x32_bf16 v[132:135], v[226:229], v[210:213], v[132:135]
	s_add_i32 m0, s99, 0x6000
	s_add_i32 s65, s14, 0xfffe0000
	buffer_load_dwordx4 v187, s[4:7], s65 offen lds
	v_mfma_f32_16x16x32_bf16 v[128:131], v[230:233], v[210:213], v[128:131]
	v_mfma_f32_16x16x32_bf16 v[120:123], v[222:225], v[214:217], v[120:123]
	v_mfma_f32_16x16x32_bf16 v[116:119], v[226:229], v[214:217], v[116:119]
	v_mfma_f32_16x16x32_bf16 v[112:115], v[230:233], v[214:217], v[112:115]
	s_add_i32 m0, s99, 0x8000
	s_nop 0
	buffer_load_dwordx4 v187, s[4:7], s14 offen lds
	v_mfma_f32_16x16x32_bf16 v[96:99], v[230:233], v[218:221], v[80:83]
	ds_read_b128 v[80:83], v178 offset:0x1000
	ds_read_b128 v[84:87], v182 offset:0x1800
	v_mfma_f32_16x16x32_bf16 v[88:91], v[234:237], v[218:221], v[238:241]
	s_add_i32 s2, s2, 2
	s_add_i32 s3, s3, 0x100000
	s_addk_i32 s14, 0x100
	s_cmp_lt_u32 s2, 11
	s_cbranch_scc1 .LBB0_1430
	ds_read_b128 v[202:205], v180 offset:0
	ds_read_b128 v[206:209], v180 offset:0x2000
	ds_read_b128 v[210:213], v180 offset:0x4000
	ds_read_b128 v[214:217], v180 offset:0x6000
	ds_read_b128 v[218:221], v180 offset:0x8000
	ds_read_b128 v[222:225], v182 offset:0
	ds_read_b128 v[226:229], v178 offset:0x800
	ds_read_b128 v[230:233], v182 offset:0x1000
	ds_read_b128 v[234:237], v178 offset:0x1800
	s_waitcnt lgkmcnt(9)
	s_nop 0
	v_mfma_f32_16x16x32_bf16 v[168:171], v[68:71], v[92:95], v[168:171]
	v_mfma_f32_16x16x32_bf16 v[164:167], v[72:75], v[92:95], v[164:167]
	v_mfma_f32_16x16x32_bf16 v[160:163], v[80:83], v[92:95], v[160:163]
	v_mfma_f32_16x16x32_bf16 v[92:95], v[84:87], v[92:95], v[156:159]
	v_mfma_f32_16x16x32_bf16 v[152:155], v[68:71], v[76:79], v[152:155]
	v_mfma_f32_16x16x32_bf16 v[148:151], v[72:75], v[76:79], v[148:151]
	v_mfma_f32_16x16x32_bf16 v[144:147], v[80:83], v[76:79], v[144:147]
	v_mfma_f32_16x16x32_bf16 v[76:79], v[84:87], v[76:79], v[140:143]
	v_mfma_f32_16x16x32_bf16 v[136:139], v[68:71], v[64:67], v[136:139]
	v_mfma_f32_16x16x32_bf16 v[132:135], v[72:75], v[64:67], v[132:135]
	v_mfma_f32_16x16x32_bf16 v[128:131], v[80:83], v[64:67], v[128:131]
	v_mfma_f32_16x16x32_bf16 v[124:127], v[84:87], v[64:67], v[124:127]
	v_mfma_f32_16x16x32_bf16 v[120:123], v[68:71], v[60:63], v[120:123]
	v_mfma_f32_16x16x32_bf16 v[116:119], v[72:75], v[60:63], v[116:119]
	v_mfma_f32_16x16x32_bf16 v[112:115], v[80:83], v[60:63], v[112:115]
	v_mfma_f32_16x16x32_bf16 v[108:111], v[84:87], v[60:63], v[108:111]
	v_mfma_f32_16x16x32_bf16 v[104:107], v[68:71], v[56:59], v[104:107]
	v_mfma_f32_16x16x32_bf16 v[140:143], v[72:75], v[56:59], v[100:103]
	v_mfma_f32_16x16x32_bf16 v[156:159], v[80:83], v[56:59], v[96:99]
	v_mfma_f32_16x16x32_bf16 v[238:241], v[84:87], v[56:59], v[88:91]
	s_waitcnt vmcnt(0)
	v_cvt_pk_bf16_f32 v36, v242, v246
	v_cvt_pk_bf16_f32 v37, v250, v188
	ds_write_b64 v197, v[36:37]
	v_cvt_pk_bf16_f32 v36, v243, v247
	v_cvt_pk_bf16_f32 v37, v251, v189
	ds_write_b64 v198, v[36:37]
	v_cvt_pk_bf16_f32 v36, v244, v248
	v_cvt_pk_bf16_f32 v37, v252, v190
	ds_write_b64 v199, v[36:37]
	v_cvt_pk_bf16_f32 v36, v245, v249
	v_cvt_pk_bf16_f32 v37, v253, v191
	ds_write_b64 v200, v[36:37]
	s_waitcnt lgkmcnt(0)
	s_barrier
	s_nop 0
	v_mfma_f32_16x16x32_bf16 v[56:59], v[226:229], v[206:209], v[148:151]
	ds_read_b128 v[148:151], v177 offset:0
	v_mfma_f32_16x16x32_bf16 v[60:63], v[230:233], v[206:209], v[144:147]
	ds_read_b128 v[144:147], v177 offset:0x2000
	v_mfma_f32_16x16x32_bf16 v[80:83], v[234:237], v[210:213], v[124:127]
	ds_read_b128 v[124:127], v177 offset:0x4000
	v_mfma_f32_16x16x32_bf16 v[88:91], v[226:229], v[214:217], v[116:119]
	ds_read_b128 v[116:119], v177 offset:0x6000
	v_mfma_f32_16x16x32_bf16 v[96:99], v[234:237], v[214:217], v[108:111]
	ds_read_b128 v[108:111], v177 offset:0x8000
	v_mfma_f32_16x16x32_bf16 v[84:87], v[222:225], v[214:217], v[120:123]
	ds_read_b128 v[120:123], v179 offset:0
	v_mfma_f32_16x16x32_bf16 v[64:67], v[234:237], v[206:209], v[76:79]
	v_mfma_f32_16x16x32_bf16 v[76:79], v[230:233], v[210:213], v[128:131]
	ds_read_b128 v[128:131], v183 offset:0x800
	v_mfma_f32_16x16x32_bf16 v[20:23], v[222:225], v[202:205], v[168:171]
	v_mfma_f32_16x16x32_bf16 v[24:27], v[226:229], v[202:205], v[164:167]
	v_mfma_f32_16x16x32_bf16 v[28:31], v[230:233], v[202:205], v[160:163]
	v_mfma_f32_16x16x32_bf16 v[32:35], v[234:237], v[202:205], v[92:95]
	v_mfma_f32_16x16x32_bf16 v[52:55], v[222:225], v[206:209], v[152:155]
	v_mfma_f32_16x16x32_bf16 v[68:71], v[222:225], v[210:213], v[136:139]
	v_mfma_f32_16x16x32_bf16 v[72:75], v[226:229], v[210:213], v[132:135]
	ds_read_b128 v[132:135], v179 offset:0x1000
	ds_read_b128 v[136:139], v183 offset:0x1800
	v_mfma_f32_16x16x32_bf16 v[92:95], v[230:233], v[214:217], v[112:115]
	v_mfma_f32_16x16x32_bf16 v[100:103], v[222:225], v[218:221], v[104:107]
	v_mfma_f32_16x16x32_bf16 v[104:107], v[226:229], v[218:221], v[140:143]
	v_mfma_f32_16x16x32_bf16 v[112:115], v[230:233], v[218:221], v[156:159]
	v_mfma_f32_16x16x32_bf16 v[140:143], v[234:237], v[218:221], v[238:241]
	s_add_i32 s2, s63, 0x140
	s_cmp_ge_i32 s2, s54
	s_cselect_b64 s[2:3], -1, 0
	s_and_b64 s[2:3], s[20:21], s[2:3]
	v_mov_b64_e32 v[50:51], v[6:7]
	v_mov_b64_e32 v[46:47], v[10:11]
	v_mov_b64_e32 v[42:43], v[14:15]
	v_mov_b64_e32 v[38:39], v[18:19]
	s_andn2_b64 vcc, exec, s[2:3]
	v_mov_b64_e32 v[48:49], v[4:5]
	v_mov_b64_e32 v[44:45], v[8:9]
	v_mov_b64_e32 v[40:41], v[12:13]
	v_mov_b64_e32 v[36:37], v[16:17]
	s_cbranch_vccnz .LBB0_1433
	s_mov_b32 s14, s10
	s_mov_b32 s15, s11
	buffer_load_dwordx4 v[48:51], v173, s[12:15], 0 offen
	buffer_load_dwordx4 v[44:47], v173, s[12:15], s43 offen
	buffer_load_dwordx4 v[40:43], v173, s[12:15], s44 offen
	buffer_load_dwordx4 v[36:39], v173, s[12:15], s45 offen

.LBB0_1437:
	s_lshl_b32 s2, s22, 11
	s_add_i32 s5, s2, s37
	s_or_b32 s2, s5, s57
	s_lshl_b32 s2, s2, 1
	v_cvt_pk_bf16_f32 v64, v64, v65
	v_cvt_pk_bf16_f32 v65, v66, v67
	s_add_i32 s14, s2, s29
	s_mov_b32 s2, s10
	s_mov_b32 s3, s11
	buffer_store_dwordx2 v[64:65], v201, s[0:3], s14 offen
	s_or_b32 s14, s5, s58
	s_lshl_b32 s14, s14, 1
	v_cvt_pk_bf16_f32 v60, v60, v61
	v_cvt_pk_bf16_f32 v61, v62, v63
	s_add_i32 s14, s14, s29
	buffer_store_dwordx2 v[60:61], v201, s[0:3], s14 offen
	s_or_b32 s14, s5, s59
	s_or_b32 s5, s5, s62
	s_lshl_b32 s14, s14, 1
	s_lshl_b32 s5, s5, 1
	v_cvt_pk_bf16_f32 v56, v56, v57
	v_cvt_pk_bf16_f32 v57, v58, v59
	s_add_i32 s14, s14, s29
	v_cvt_pk_bf16_f32 v52, v52, v53
	v_cvt_pk_bf16_f32 v53, v54, v55
	s_add_i32 s5, s5, s29
	buffer_store_dwordx2 v[56:57], v201, s[0:3], s14 offen
	buffer_store_dwordx2 v[52:53], v201, s[0:3], s5 offen

.LBB0_1442:
	buffer_load_dwordx4 v[242:245], v173, s[8:11], s42 offen
	buffer_load_dwordx4 v[246:249], v173, s[8:11], s51 offen
	buffer_load_dwordx4 v[250:253], v173, s[8:11], s52 offen
	buffer_load_dwordx4 v[188:191], v173, s[8:11], s53 offen
	s_waitcnt vmcnt(4)
	ds_write_b128 v184, v[36:39]
	ds_write_b128 v184, v[40:43] offset:8192
	ds_write_b128 v184, v[44:47] offset:16384
	ds_write_b128 v184, v[48:51] offset:24576
	v_cvt_pk_bf16_f32 v36, v32, v28
	v_cvt_pk_bf16_f32 v37, v24, v20
	ds_write_b64 v3, v[36:37] offset:49152
	v_cvt_pk_bf16_f32 v20, v33, v29
	v_cvt_pk_bf16_f32 v21, v25, v21
	ds_write_b64 v194, v[20:21] offset:49280
	v_cvt_pk_bf16_f32 v20, v34, v30
	v_cvt_pk_bf16_f32 v21, v26, v22
	ds_write_b64 v195, v[20:21] offset:49408
	v_cvt_pk_bf16_f32 v52, v35, v31
	v_cvt_pk_bf16_f32 v53, v27, v23
	ds_write_b64 v196, v[52:53] offset:49536
	s_waitcnt lgkmcnt(0)
	s_barrier
	s_mov_b32 m0, s99
	s_nop 0
	buffer_load_dwordx4 v187, s[4:7], s46 offen lds
	s_add_i32 m0, s99, 0x2000
	s_nop 0
	buffer_load_dwordx4 v187, s[4:7], s47 offen lds
	s_add_i32 m0, s99, 0x4000
	s_nop 0
	buffer_load_dwordx4 v187, s[4:7], s48 offen lds
	s_add_i32 m0, s99, 0x6000
	s_nop 0
	buffer_load_dwordx4 v187, s[4:7], s49 offen lds
	ds_read_b128 v[72:75], v176 offset:0
	ds_read_b128 v[60:63], v176 offset:0x2000
	ds_read_b128 v[56:59], v176 offset:0x4000
	ds_read_b128 v[52:55], v176 offset:0x6000
	ds_read_b128 v[64:67], v178 offset:0
	ds_read_b128 v[68:71], v182 offset:0x800
	ds_read_b128 v[76:79], v178 offset:0x1000
	ds_read_b128 v[80:83], v182 offset:0x1800
	v_mov_b32_e32 v84, 0
	s_mov_b32 s2, -2
	s_mov_b32 s3, 0x186000
	s_mov_b32 s14, 0x60180
	v_mov_b32_e32 v85, v84
	v_mov_b32_e32 v86, v84
	v_mov_b32_e32 v87, v84
	v_mov_b32_e32 v88, v84
	v_mov_b32_e32 v89, v84
	v_mov_b32_e32 v90, v84
	v_mov_b32_e32 v91, v84
	v_mov_b32_e32 v92, v84
	v_mov_b32_e32 v93, v84
	v_mov_b32_e32 v94, v84
	v_mov_b32_e32 v95, v84
	v_mov_b32_e32 v96, v84
	v_mov_b32_e32 v97, v84
	v_mov_b32_e32 v98, v84
	v_mov_b32_e32 v99, v84
	v_mov_b32_e32 v100, v84
	v_mov_b32_e32 v101, v84
	v_mov_b32_e32 v102, v84
	v_mov_b32_e32 v103, v84
	v_mov_b32_e32 v104, v84
	v_mov_b32_e32 v105, v84
	v_mov_b32_e32 v106, v84
	v_mov_b32_e32 v107, v84
	v_mov_b32_e32 v108, v84
	v_mov_b32_e32 v109, v84
	v_mov_b32_e32 v110, v84
	v_mov_b32_e32 v111, v84
	v_mov_b32_e32 v112, v84
	v_mov_b32_e32 v113, v84
	v_mov_b32_e32 v114, v84
	v_mov_b32_e32 v115, v84
	v_mov_b32_e32 v116, v84
	v_mov_b32_e32 v117, v84
	v_mov_b32_e32 v118, v84
	v_mov_b32_e32 v119, v84
	v_mov_b32_e32 v120, v84
	v_mov_b32_e32 v121, v84
	v_mov_b32_e32 v122, v84
	v_mov_b32_e32 v123, v84
	v_mov_b32_e32 v124, v84
	v_mov_b32_e32 v125, v84
	v_mov_b32_e32 v126, v84
	v_mov_b32_e32 v127, v84
	v_mov_b32_e32 v128, v84
	v_mov_b32_e32 v129, v84
	v_mov_b32_e32 v130, v84
	v_mov_b32_e32 v131, v84
	v_mov_b32_e32 v132, v84
	v_mov_b32_e32 v133, v84
	v_mov_b32_e32 v134, v84
	v_mov_b32_e32 v135, v84
	v_mov_b32_e32 v136, v84
	v_mov_b32_e32 v137, v84
	v_mov_b32_e32 v138, v84
	v_mov_b32_e32 v139, v84
	v_mov_b32_e32 v140, v84
	v_mov_b32_e32 v141, v84
	v_mov_b32_e32 v142, v84
	v_mov_b32_e32 v143, v84
	v_mov_b32_e32 v144, v84
	v_mov_b32_e32 v145, v84
	v_mov_b32_e32 v146, v84
	v_mov_b32_e32 v147, v84
.LBB0_1443:
	ds_read_b128 v[148:151], v180 offset:0
	ds_read_b128 v[152:155], v180 offset:0x2000
	ds_read_b128 v[156:159], v180 offset:0x4000
	ds_read_b128 v[160:163], v180 offset:0x6000
	ds_read_b128 v[164:167], v182 offset:0
	ds_read_b128 v[168:171], v178 offset:0x800
	ds_read_b128 v[202:205], v182 offset:0x1000
	ds_read_b128 v[206:209], v178 offset:0x1800
	s_waitcnt lgkmcnt(8)
	s_nop 1
	v_mfma_f32_16x16x32_bf16 v[144:147], v[64:67], v[72:75], v[144:147]
	v_mfma_f32_16x16x32_bf16 v[140:143], v[68:71], v[72:75], v[140:143]
	s_add_i32 s15, s3, 0xfff7a000
	buffer_load_dwordx4 v[24:27], v173, s[8:11], s15 offen
	v_mfma_f32_16x16x32_bf16 v[136:139], v[76:79], v[72:75], v[136:139]
	v_mfma_f32_16x16x32_bf16 v[72:75], v[80:83], v[72:75], v[132:135]
	v_mfma_f32_16x16x32_bf16 v[128:131], v[64:67], v[60:63], v[128:131]
	v_mfma_f32_16x16x32_bf16 v[124:127], v[68:71], v[60:63], v[124:127]
	s_add_i32 s23, s3, 0xfff7c000
	buffer_load_dwordx4 v[32:35], v173, s[8:11], s23 offen
	v_mfma_f32_16x16x32_bf16 v[120:123], v[76:79], v[60:63], v[120:123]
	v_mfma_f32_16x16x32_bf16 v[60:63], v[80:83], v[60:63], v[116:119]
	v_mfma_f32_16x16x32_bf16 v[112:115], v[64:67], v[56:59], v[112:115]
	v_mfma_f32_16x16x32_bf16 v[108:111], v[68:71], v[56:59], v[108:111]
	s_add_i32 s15, s3, 0xfff7e000
	buffer_load_dwordx4 v[20:23], v173, s[8:11], s15 offen
	v_mfma_f32_16x16x32_bf16 v[104:107], v[76:79], v[56:59], v[104:107]
	v_mfma_f32_16x16x32_bf16 v[56:59], v[80:83], v[56:59], v[100:103]
	v_mfma_f32_16x16x32_bf16 v[64:67], v[64:67], v[52:55], v[96:99]
	v_mfma_f32_16x16x32_bf16 v[68:71], v[68:71], v[52:55], v[92:95]
	s_add_i32 s23, s3, 0xfff80000
	buffer_load_dwordx4 v[28:31], v173, s[8:11], s23 offen
	v_mfma_f32_16x16x32_bf16 v[76:79], v[76:79], v[52:55], v[88:91]
	v_mfma_f32_16x16x32_bf16 v[52:55], v[80:83], v[52:55], v[84:87]
	s_waitcnt vmcnt(4)
	v_cvt_pk_bf16_f32 v36, v242, v246
	v_cvt_pk_bf16_f32 v37, v250, v188
	ds_write_b64 v197, v[36:37]
	v_cvt_pk_bf16_f32 v36, v243, v247
	v_cvt_pk_bf16_f32 v37, v251, v189
	ds_write_b64 v198, v[36:37]
	v_cvt_pk_bf16_f32 v36, v244, v248
	v_cvt_pk_bf16_f32 v37, v252, v190
	ds_write_b64 v199, v[36:37]
	v_cvt_pk_bf16_f32 v36, v245, v249
	v_cvt_pk_bf16_f32 v37, v253, v191
	ds_write_b64 v200, v[36:37]
	s_waitcnt lgkmcnt(0)
	s_barrier
	ds_read_b128 v[116:119], v177 offset:0
	s_nop 0
	v_mfma_f32_16x16x32_bf16 v[100:103], v[202:205], v[152:155], v[120:123]
	ds_read_b128 v[120:123], v177 offset:0x2000
	v_mfma_f32_16x16x32_bf16 v[96:99], v[168:171], v[152:155], v[124:127]
	s_mov_b32 m0, s98
	s_add_i32 s15, s14, 0xfff9ff80
	buffer_load_dwordx4 v187, s[4:7], s15 offen lds
	ds_read_b128 v[124:127], v177 offset:0x4000
	v_mfma_f32_16x16x32_bf16 v[92:95], v[164:167], v[152:155], v[128:131]
	ds_read_b128 v[128:131], v177 offset:0x6000
	ds_read_b128 v[132:135], v179 offset:0
	v_mfma_f32_16x16x32_bf16 v[88:91], v[202:205], v[148:151], v[136:139]
	ds_read_b128 v[136:139], v183 offset:0x800
	v_mfma_f32_16x16x32_bf16 v[80:83], v[164:167], v[148:151], v[144:147]
	v_mfma_f32_16x16x32_bf16 v[84:87], v[168:171], v[148:151], v[140:143]
	s_add_i32 m0, s98, 0x2000
	s_add_i32 s23, s14, 0xfffbff80
	buffer_load_dwordx4 v187, s[4:7], s23 offen lds
	ds_read_b128 v[140:143], v179 offset:0x1000
	ds_read_b128 v[144:147], v183 offset:0x1800
	v_mfma_f32_16x16x32_bf16 v[72:75], v[206:209], v[148:151], v[72:75]
	v_mfma_f32_16x16x32_bf16 v[60:63], v[206:209], v[152:155], v[60:63]
	v_mfma_f32_16x16x32_bf16 v[112:115], v[164:167], v[156:159], v[112:115]
	v_mfma_f32_16x16x32_bf16 v[108:111], v[168:171], v[156:159], v[108:111]
	s_add_i32 m0, s98, 0x4000
	s_add_i32 s15, s14, 0xfffdff80
	buffer_load_dwordx4 v187, s[4:7], s15 offen lds
	v_mfma_f32_16x16x32_bf16 v[104:107], v[202:205], v[156:159], v[104:107]
	v_mfma_f32_16x16x32_bf16 v[56:59], v[206:209], v[156:159], v[56:59]
	v_mfma_f32_16x16x32_bf16 v[64:67], v[164:167], v[160:163], v[64:67]
	v_mfma_f32_16x16x32_bf16 v[68:71], v[168:171], v[160:163], v[68:71]
	s_add_i32 m0, s98, 0x6000
	s_add_i32 s23, s14, 0xffffff80
	buffer_load_dwordx4 v187, s[4:7], s23 offen lds
	v_mfma_f32_16x16x32_bf16 v[76:79], v[202:205], v[160:163], v[76:79]
	v_mfma_f32_16x16x32_bf16 v[52:55], v[206:209], v[160:163], v[52:55]
	ds_read_b128 v[148:151], v181 offset:0
	ds_read_b128 v[152:155], v181 offset:0x2000
	ds_read_b128 v[156:159], v181 offset:0x4000
	ds_read_b128 v[160:163], v181 offset:0x6000
	ds_read_b128 v[164:167], v183 offset:0
	ds_read_b128 v[168:171], v179 offset:0x800
	ds_read_b128 v[202:205], v183 offset:0x1000
	ds_read_b128 v[206:209], v179 offset:0x1800
	s_waitcnt lgkmcnt(8)
	s_nop 0
	v_mfma_f32_16x16x32_bf16 v[80:83], v[132:135], v[116:119], v[80:83]
	v_mfma_f32_16x16x32_bf16 v[84:87], v[136:139], v[116:119], v[84:87]
	s_add_i32 s15, s3, 0xffffa000
	buffer_load_dwordx4 v[242:245], v173, s[8:11], s15 offen
	v_mfma_f32_16x16x32_bf16 v[88:91], v[140:143], v[116:119], v[88:91]
	v_mfma_f32_16x16x32_bf16 v[72:75], v[144:147], v[116:119], v[72:75]
	v_mfma_f32_16x16x32_bf16 v[92:95], v[132:135], v[120:123], v[92:95]
	v_mfma_f32_16x16x32_bf16 v[96:99], v[136:139], v[120:123], v[96:99]
	s_add_i32 s23, s3, 0xffffc000
	buffer_load_dwordx4 v[246:249], v173, s[8:11], s23 offen
	v_mfma_f32_16x16x32_bf16 v[100:103], v[140:143], v[120:123], v[100:103]
	v_mfma_f32_16x16x32_bf16 v[60:63], v[144:147], v[120:123], v[60:63]
	v_mfma_f32_16x16x32_bf16 v[112:115], v[132:135], v[124:127], v[112:115]
	v_mfma_f32_16x16x32_bf16 v[108:111], v[136:139], v[124:127], v[108:111]
	s_add_i32 s15, s3, 0xffffe000
	buffer_load_dwordx4 v[250:253], v173, s[8:11], s15 offen
	v_mfma_f32_16x16x32_bf16 v[104:107], v[140:143], v[124:127], v[104:107]
	v_mfma_f32_16x16x32_bf16 v[56:59], v[144:147], v[124:127], v[56:59]
	v_mfma_f32_16x16x32_bf16 v[64:67], v[132:135], v[128:131], v[64:67]
	v_mfma_f32_16x16x32_bf16 v[68:71], v[136:139], v[128:131], v[68:71]
	buffer_load_dwordx4 v[188:191], v173, s[8:11], s3 offen
	v_mfma_f32_16x16x32_bf16 v[76:79], v[140:143], v[128:131], v[76:79]
	v_mfma_f32_16x16x32_bf16 v[210:213], v[144:147], v[128:131], v[52:55]
	s_waitcnt vmcnt(4)
	v_cvt_pk_bf16_f32 v36, v24, v32
	v_cvt_pk_bf16_f32 v37, v20, v28
	ds_write_b64 v3, v[36:37] offset:49152
	v_cvt_pk_bf16_f32 v36, v25, v33
	v_cvt_pk_bf16_f32 v37, v21, v29
	ds_write_b64 v194, v[36:37] offset:49280
	v_cvt_pk_bf16_f32 v36, v26, v34
	v_cvt_pk_bf16_f32 v37, v22, v30
	ds_write_b64 v195, v[36:37] offset:49408
	v_cvt_pk_bf16_f32 v36, v27, v35
	v_cvt_pk_bf16_f32 v37, v23, v31
	ds_write_b64 v196, v[36:37] offset:49536
	s_waitcnt lgkmcnt(0)
	s_barrier
	s_nop 0
	v_mfma_f32_16x16x32_bf16 v[132:135], v[206:209], v[148:151], v[72:75]
	ds_read_b128 v[72:75], v176 offset:0
	v_mfma_f32_16x16x32_bf16 v[116:119], v[206:209], v[152:155], v[60:63]
	s_mov_b32 m0, s99
	s_add_i32 s15, s14, 0xfffa0000
	buffer_load_dwordx4 v187, s[4:7], s15 offen lds
	ds_read_b128 v[60:63], v176 offset:0x2000
	v_mfma_f32_16x16x32_bf16 v[120:123], v[202:205], v[152:155], v[100:103]
	v_mfma_f32_16x16x32_bf16 v[100:103], v[206:209], v[156:159], v[56:59]
	ds_read_b128 v[56:59], v176 offset:0x4000
	ds_read_b128 v[52:55], v176 offset:0x6000
	v_mfma_f32_16x16x32_bf16 v[124:127], v[168:171], v[152:155], v[96:99]
	v_mfma_f32_16x16x32_bf16 v[96:99], v[164:167], v[160:163], v[64:67]
	s_add_i32 m0, s99, 0x2000
	s_add_i32 s23, s14, 0xfffc0000
	buffer_load_dwordx4 v187, s[4:7], s23 offen lds
	ds_read_b128 v[64:67], v178 offset:0
	v_mfma_f32_16x16x32_bf16 v[128:131], v[164:167], v[152:155], v[92:95]
	v_mfma_f32_16x16x32_bf16 v[92:95], v[168:171], v[160:163], v[68:71]
	ds_read_b128 v[68:71], v182 offset:0x800
	v_mfma_f32_16x16x32_bf16 v[144:147], v[164:167], v[148:151], v[80:83]
	v_mfma_f32_16x16x32_bf16 v[140:143], v[168:171], v[148:151], v[84:87]
	s_add_i32 m0, s99, 0x4000
	s_add_i32 s15, s14, 0xfffe0000
	buffer_load_dwordx4 v187, s[4:7], s15 offen lds
	v_mfma_f32_16x16x32_bf16 v[136:139], v[202:205], v[148:151], v[88:91]
	v_mfma_f32_16x16x32_bf16 v[112:115], v[164:167], v[156:159], v[112:115]
	v_mfma_f32_16x16x32_bf16 v[108:111], v[168:171], v[156:159], v[108:111]
	v_mfma_f32_16x16x32_bf16 v[104:107], v[202:205], v[156:159], v[104:107]
	s_add_i32 m0, s99, 0x6000
	s_nop 0
	buffer_load_dwordx4 v187, s[4:7], s14 offen lds
	v_mfma_f32_16x16x32_bf16 v[88:91], v[202:205], v[160:163], v[76:79]
	ds_read_b128 v[76:79], v178 offset:0x1000
	ds_read_b128 v[80:83], v182 offset:0x1800
	v_mfma_f32_16x16x32_bf16 v[84:87], v[206:209], v[160:163], v[210:213]
	s_add_i32 s2, s2, 2
	s_add_i32 s3, s3, 0x100000
	s_addk_i32 s14, 0x100
	s_cmp_lt_u32 s2, 11
	s_cbranch_scc1 .LBB0_1443
	ds_read_b128 v[148:151], v180 offset:0
	ds_read_b128 v[152:155], v180 offset:0x2000
	ds_read_b128 v[156:159], v180 offset:0x4000
	ds_read_b128 v[160:163], v180 offset:0x6000
	ds_read_b128 v[164:167], v182 offset:0
	ds_read_b128 v[168:171], v178 offset:0x800
	ds_read_b128 v[202:205], v182 offset:0x1000
	ds_read_b128 v[206:209], v178 offset:0x1800
	s_waitcnt lgkmcnt(8)
	s_nop 0
	v_mfma_f32_16x16x32_bf16 v[144:147], v[64:67], v[72:75], v[144:147]
	v_mfma_f32_16x16x32_bf16 v[140:143], v[68:71], v[72:75], v[140:143]
	v_mfma_f32_16x16x32_bf16 v[136:139], v[76:79], v[72:75], v[136:139]
	v_mfma_f32_16x16x32_bf16 v[72:75], v[80:83], v[72:75], v[132:135]
	v_mfma_f32_16x16x32_bf16 v[128:131], v[64:67], v[60:63], v[128:131]
	v_mfma_f32_16x16x32_bf16 v[124:127], v[68:71], v[60:63], v[124:127]
	v_mfma_f32_16x16x32_bf16 v[120:123], v[76:79], v[60:63], v[120:123]
	v_mfma_f32_16x16x32_bf16 v[60:63], v[80:83], v[60:63], v[116:119]
	v_mfma_f32_16x16x32_bf16 v[112:115], v[64:67], v[56:59], v[112:115]
	v_mfma_f32_16x16x32_bf16 v[108:111], v[68:71], v[56:59], v[108:111]
	v_mfma_f32_16x16x32_bf16 v[104:107], v[76:79], v[56:59], v[104:107]
	v_mfma_f32_16x16x32_bf16 v[100:103], v[80:83], v[56:59], v[100:103]
	v_mfma_f32_16x16x32_bf16 v[96:99], v[64:67], v[52:55], v[96:99]
	v_mfma_f32_16x16x32_bf16 v[116:119], v[68:71], v[52:55], v[92:95]
	v_mfma_f32_16x16x32_bf16 v[132:135], v[76:79], v[52:55], v[88:91]
	v_mfma_f32_16x16x32_bf16 v[210:213], v[80:83], v[52:55], v[84:87]
	s_waitcnt vmcnt(0)
	v_cvt_pk_bf16_f32 v36, v242, v246
	v_cvt_pk_bf16_f32 v37, v250, v188
	ds_write_b64 v197, v[36:37]
	v_cvt_pk_bf16_f32 v36, v243, v247
	v_cvt_pk_bf16_f32 v37, v251, v189
	ds_write_b64 v198, v[36:37]
	v_cvt_pk_bf16_f32 v36, v244, v248
	v_cvt_pk_bf16_f32 v37, v252, v190
	ds_write_b64 v199, v[36:37]
	v_cvt_pk_bf16_f32 v36, v245, v249
	v_cvt_pk_bf16_f32 v37, v253, v191
	ds_write_b64 v200, v[36:37]
	s_waitcnt lgkmcnt(0)
	s_barrier
	s_nop 0
	v_mfma_f32_16x16x32_bf16 v[52:55], v[164:167], v[156:159], v[112:115]
	ds_read_b128 v[112:115], v177 offset:0
	ds_read_b128 v[92:95], v177 offset:0x2000
	ds_read_b128 v[84:87], v177 offset:0x4000
	ds_read_b128 v[76:79], v177 offset:0x6000
	ds_read_b128 v[88:91], v179 offset:0
	v_mfma_f32_16x16x32_bf16 v[68:71], v[164:167], v[160:163], v[96:99]
	ds_read_b128 v[96:99], v183 offset:0x800
	v_mfma_f32_16x16x32_bf16 v[20:23], v[164:167], v[148:151], v[144:147]
	v_mfma_f32_16x16x32_bf16 v[24:27], v[168:171], v[148:151], v[140:143]
	v_mfma_f32_16x16x32_bf16 v[28:31], v[202:205], v[148:151], v[136:139]
	v_mfma_f32_16x16x32_bf16 v[32:35], v[206:209], v[148:151], v[72:75]
	v_mfma_f32_16x16x32_bf16 v[36:39], v[164:167], v[152:155], v[128:131]
	v_mfma_f32_16x16x32_bf16 v[40:43], v[168:171], v[152:155], v[124:127]
	v_mfma_f32_16x16x32_bf16 v[44:47], v[202:205], v[152:155], v[120:123]
	v_mfma_f32_16x16x32_bf16 v[48:51], v[206:209], v[152:155], v[60:63]
	v_mfma_f32_16x16x32_bf16 v[56:59], v[168:171], v[156:159], v[108:111]
	v_mfma_f32_16x16x32_bf16 v[60:63], v[202:205], v[156:159], v[104:107]
	v_mfma_f32_16x16x32_bf16 v[64:67], v[206:209], v[156:159], v[100:103]
	ds_read_b128 v[100:103], v179 offset:0x1000
	ds_read_b128 v[104:107], v183 offset:0x1800
	v_mfma_f32_16x16x32_bf16 v[72:75], v[168:171], v[160:163], v[116:119]
	v_mfma_f32_16x16x32_bf16 v[80:83], v[202:205], v[160:163], v[132:135]
	v_mfma_f32_16x16x32_bf16 v[108:111], v[206:209], v[160:163], v[210:213]
	s_andn2_b64 vcc, exec, s[20:21]
	s_cbranch_vccnz .LBB0_1446
	s_mov_b32 s14, s10
	s_mov_b32 s15, s11
	buffer_load_dwordx4 v[4:7], v173, s[12:15], 0 offen
	buffer_load_dwordx4 v[8:11], v173, s[12:15], s43 offen
	buffer_load_dwordx4 v[12:15], v173, s[12:15], s44 offen
	buffer_load_dwordx4 v[16:19], v173, s[12:15], s45 offen

.LBB0_1449:
	s_lshl_b32 s2, s22, 11
	s_add_i32 s4, s2, s35
	s_or_b32 s2, s4, s57
	s_lshl_b32 s2, s2, 1
	v_cvt_pk_bf16_f32 v48, v48, v49
	v_cvt_pk_bf16_f32 v49, v50, v51
	s_add_i32 s5, s2, s29
	s_mov_b32 s2, s10
	s_mov_b32 s3, s11
	buffer_store_dwordx2 v[48:49], v201, s[0:3], s5 offen
	s_or_b32 s5, s4, s58
	s_lshl_b32 s5, s5, 1
	v_cvt_pk_bf16_f32 v44, v44, v45
	v_cvt_pk_bf16_f32 v45, v46, v47
	s_add_i32 s5, s5, s29
	buffer_store_dwordx2 v[44:45], v201, s[0:3], s5 offen
	s_or_b32 s5, s4, s59
	s_or_b32 s4, s4, s62
	s_lshl_b32 s5, s5, 1
	s_lshl_b32 s4, s4, 1
	v_cvt_pk_bf16_f32 v40, v40, v41
	v_cvt_pk_bf16_f32 v41, v42, v43
	s_add_i32 s5, s5, s29
	v_cvt_pk_bf16_f32 v36, v36, v37
	v_cvt_pk_bf16_f32 v37, v38, v39
	s_add_i32 s4, s4, s29
	buffer_store_dwordx2 v[40:41], v201, s[0:3], s5 offen
	buffer_store_dwordx2 v[36:37], v201, s[0:3], s4 offen

.LBB0_1453:
	s_lshl_b32 s2, s22, 11
	s_add_i32 s4, s5, s2
	s_or_b32 s2, s4, s57
	s_lshl_b32 s2, s2, 1
	v_cvt_pk_bf16_f32 v4, v32, v33
	v_cvt_pk_bf16_f32 v5, v34, v35
	s_add_i32 s5, s2, s29
	s_mov_b32 s2, s10
	s_mov_b32 s3, s11
	buffer_store_dwordx2 v[4:5], v201, s[0:3], s5 offen
	s_or_b32 s5, s4, s58
	s_lshl_b32 s5, s5, 1
	v_cvt_pk_bf16_f32 v4, v28, v29
	v_cvt_pk_bf16_f32 v5, v30, v31
	s_add_i32 s5, s5, s29
	buffer_store_dwordx2 v[4:5], v201, s[0:3], s5 offen
	s_or_b32 s5, s4, s59
	s_lshl_b32 s5, s5, 1
	s_or_b32 s4, s4, s62
	v_cvt_pk_bf16_f32 v4, v24, v25
	v_cvt_pk_bf16_f32 v5, v26, v27
	s_add_i32 s5, s5, s29
	s_lshl_b32 s4, s4, 1
	buffer_store_dwordx2 v[4:5], v201, s[0:3], s5 offen
	v_cvt_pk_bf16_f32 v4, v20, v21
	v_cvt_pk_bf16_f32 v5, v22, v23
	s_add_i32 s4, s4, s29
	buffer_store_dwordx2 v[4:5], v201, s[0:3], s4 offen
	s_addk_i32 s63, 0x140
	s_cmp_lt_i32 s63, s54
	s_cbranch_scc0 .LBB0_1418

.LBB0_1455:
	s_lshl_b32 s2, s22, 11
	s_add_i32 s5, s2, s28
	s_or_b32 s2, s5, s57
	s_lshl_b32 s2, s2, 1
	v_cvt_pk_bf16_f32 v112, v112, v113
	v_cvt_pk_bf16_f32 v113, v114, v115
	s_add_i32 s14, s2, s29
	s_mov_b32 s2, s10
	s_mov_b32 s3, s11
	buffer_store_dwordx2 v[112:113], v201, s[0:3], s14 offen
	s_or_b32 s14, s5, s58
	s_lshl_b32 s14, s14, 1
	v_cvt_pk_bf16_f32 v108, v108, v109
	v_cvt_pk_bf16_f32 v109, v110, v111
	s_add_i32 s14, s14, s29
	buffer_store_dwordx2 v[108:109], v201, s[0:3], s14 offen
	s_or_b32 s14, s5, s59
	s_or_b32 s5, s5, s62
	s_lshl_b32 s14, s14, 1
	s_lshl_b32 s5, s5, 1
	v_cvt_pk_bf16_f32 v104, v104, v105
	v_cvt_pk_bf16_f32 v105, v106, v107
	s_add_i32 s14, s14, s29
	v_cvt_pk_bf16_f32 v100, v100, v101
	v_cvt_pk_bf16_f32 v101, v102, v103
	s_add_i32 s5, s5, s29
	buffer_store_dwordx2 v[104:105], v201, s[0:3], s14 offen
	buffer_store_dwordx2 v[100:101], v201, s[0:3], s5 offen
	s_cmp_ge_u32 s30, s64
	s_cbranch_scc1 .LBB0_1435
.LBB0_1456:
	s_lshl_b32 s2, s22, 11
	s_add_i32 s5, s2, s31
	s_or_b32 s2, s5, s57
	s_lshl_b32 s2, s2, 1
	v_cvt_pk_bf16_f32 v96, v96, v97
	v_cvt_pk_bf16_f32 v97, v98, v99
	s_add_i32 s14, s2, s29
	s_mov_b32 s2, s10
	s_mov_b32 s3, s11
	buffer_store_dwordx2 v[96:97], v201, s[0:3], s14 offen
	s_or_b32 s14, s5, s58
	s_lshl_b32 s14, s14, 1
	v_cvt_pk_bf16_f32 v92, v92, v93
	v_cvt_pk_bf16_f32 v93, v94, v95
	s_add_i32 s14, s14, s29
	buffer_store_dwordx2 v[92:93], v201, s[0:3], s14 offen
	s_or_b32 s14, s5, s59
	s_or_b32 s5, s5, s62
	s_lshl_b32 s14, s14, 1
	s_lshl_b32 s5, s5, 1
	v_cvt_pk_bf16_f32 v88, v88, v89
	v_cvt_pk_bf16_f32 v89, v90, v91
	s_add_i32 s14, s14, s29
	v_cvt_pk_bf16_f32 v84, v84, v85
	v_cvt_pk_bf16_f32 v85, v86, v87
	s_add_i32 s5, s5, s29
	buffer_store_dwordx2 v[88:89], v201, s[0:3], s14 offen
	buffer_store_dwordx2 v[84:85], v201, s[0:3], s5 offen
	s_cmp_ge_u32 s34, s64
	s_cbranch_scc1 .LBB0_1436
.LBB0_1457:
	s_lshl_b32 s2, s22, 11
	s_add_i32 s5, s2, s35
	s_or_b32 s2, s5, s57
	s_lshl_b32 s2, s2, 1
	v_cvt_pk_bf16_f32 v80, v80, v81
	v_cvt_pk_bf16_f32 v81, v82, v83
	s_add_i32 s14, s2, s29
	s_mov_b32 s2, s10
	s_mov_b32 s3, s11
	buffer_store_dwordx2 v[80:81], v201, s[0:3], s14 offen
	s_or_b32 s14, s5, s58
	s_lshl_b32 s14, s14, 1
	v_cvt_pk_bf16_f32 v76, v76, v77
	v_cvt_pk_bf16_f32 v77, v78, v79
	s_add_i32 s14, s14, s29
	buffer_store_dwordx2 v[76:77], v201, s[0:3], s14 offen
	s_or_b32 s14, s5, s59
	s_or_b32 s5, s5, s62
	s_lshl_b32 s14, s14, 1
	s_lshl_b32 s5, s5, 1
	v_cvt_pk_bf16_f32 v72, v72, v73
	v_cvt_pk_bf16_f32 v73, v74, v75
	s_add_i32 s14, s14, s29
	v_cvt_pk_bf16_f32 v68, v68, v69
	v_cvt_pk_bf16_f32 v69, v70, v71
	s_add_i32 s5, s5, s29
	buffer_store_dwordx2 v[72:73], v201, s[0:3], s14 offen
	buffer_store_dwordx2 v[68:69], v201, s[0:3], s5 offen
	s_cmp_ge_u32 s36, s64
	s_cbranch_scc0 .LBB0_1437
	s_branch .LBB0_1438
.LBB0_1458:
	s_lshl_b32 s2, s22, 11
	s_add_i32 s4, s2, s28
	s_or_b32 s2, s4, s57
	s_lshl_b32 s2, s2, 1
	v_cvt_pk_bf16_f32 v80, v80, v81
	v_cvt_pk_bf16_f32 v81, v82, v83
	s_add_i32 s5, s2, s29
	s_mov_b32 s2, s10
	s_mov_b32 s3, s11
	buffer_store_dwordx2 v[80:81], v201, s[0:3], s5 offen
	s_or_b32 s5, s4, s58
	s_lshl_b32 s5, s5, 1
	v_cvt_pk_bf16_f32 v76, v76, v77
	v_cvt_pk_bf16_f32 v77, v78, v79
	s_add_i32 s5, s5, s29
	buffer_store_dwordx2 v[76:77], v201, s[0:3], s5 offen
	s_or_b32 s5, s4, s59
	s_or_b32 s4, s4, s62
	s_lshl_b32 s5, s5, 1
	s_lshl_b32 s4, s4, 1
	v_cvt_pk_bf16_f32 v72, v72, v73
	v_cvt_pk_bf16_f32 v73, v74, v75
	s_add_i32 s5, s5, s29
	v_cvt_pk_bf16_f32 v68, v68, v69
	v_cvt_pk_bf16_f32 v69, v70, v71
	s_add_i32 s4, s4, s29
	buffer_store_dwordx2 v[72:73], v201, s[0:3], s5 offen
	buffer_store_dwordx2 v[68:69], v201, s[0:3], s4 offen
	s_cmp_ge_u32 s30, s64
	s_cbranch_scc1 .LBB0_1448
.LBB0_1459:
	s_lshl_b32 s2, s22, 11
	s_add_i32 s4, s2, s31
	s_or_b32 s2, s4, s57
	s_lshl_b32 s2, s2, 1
	v_cvt_pk_bf16_f32 v64, v64, v65
	v_cvt_pk_bf16_f32 v65, v66, v67
	s_add_i32 s5, s2, s29
	s_mov_b32 s2, s10
	s_mov_b32 s3, s11
	buffer_store_dwordx2 v[64:65], v201, s[0:3], s5 offen
	s_or_b32 s5, s4, s58
	s_lshl_b32 s5, s5, 1
	v_cvt_pk_bf16_f32 v60, v60, v61
	v_cvt_pk_bf16_f32 v61, v62, v63
	s_add_i32 s5, s5, s29
	buffer_store_dwordx2 v[60:61], v201, s[0:3], s5 offen
	s_or_b32 s5, s4, s59
	s_or_b32 s4, s4, s62
	s_lshl_b32 s5, s5, 1
	s_lshl_b32 s4, s4, 1
	v_cvt_pk_bf16_f32 v56, v56, v57
	v_cvt_pk_bf16_f32 v57, v58, v59
	s_add_i32 s5, s5, s29
	v_cvt_pk_bf16_f32 v52, v52, v53
	v_cvt_pk_bf16_f32 v53, v54, v55
	s_add_i32 s4, s4, s29
	buffer_store_dwordx2 v[56:57], v201, s[0:3], s5 offen
	buffer_store_dwordx2 v[52:53], v201, s[0:3], s4 offen
	s_cmp_ge_u32 s34, s64
	s_cbranch_scc0 .LBB0_1449
	s_branch .LBB0_1450
